# L1/L2: node-range split uses (blockIdx*N)>>8 (frozen 256-WG grid) instead of 64-bit software division
# speedup vs baseline: 1.0204x; 1.0204x over previous
_Z7k_layerILi1EEvPKDF16_PKiPKjS3_S3_S1_PKfPDF16_PhS3_S7_Pf:
	s_load_dwordx2 s[24:25], s[0:1], 0x50
	s_load_dwordx8 s[8:15], s[0:1], 0x0
	s_load_dwordx8 s[16:23], s[0:1], 0x20
	v_lshrrev_b32_e32 v2, 5, v0
	v_and_b32_e32 v4, 31, v0
	v_mul_u32_u24_e32 v3, 0x210, v2
	v_lshlrev_b32_e32 v5, 4, v4
	v_or_b32_e32 v1, 0xfffffc00, v0
	v_add3_u32 v4, v3, v5, 0
	v_lshl_or_b32 v2, v2, 9, v5
	v_mov_b32_e32 v3, 0
	s_waitcnt lgkmcnt(0)
	v_add_u32_e32 v3, 0x4000, v2
	v_lshlrev_b32_e32 v30, 4, v0
	v_cmp_gt_u32_e32 vcc, 16, v0
	s_and_saveexec_b64 s[4:5], vcc
	global_load_dwordx4 v[34:37], v30, s[20:21]
	s_mov_b64 exec, s[4:5]
	global_load_dwordx4 v[6:9], v2, s[18:19]
	global_load_dwordx4 v[10:13], v3, s[18:19]
	v_add_u32_e32 v31, 0x4000, v30
	v_add_u32_e32 v32, 0x8000, v30
	v_add_u32_e32 v33, 0xc000, v30
	global_load_dwordx4 v[14:17], v30, s[8:9]
	global_load_dwordx4 v[18:21], v31, s[8:9]
	global_load_dwordx4 v[22:25], v32, s[8:9]
	global_load_dwordx4 v[26:29], v33, s[8:9]
	v_add_u32_e32 v5, 0xcc10, v30
	s_waitcnt vmcnt(5)
	ds_write_b128 v4, v[6:9]
	s_waitcnt vmcnt(4)
	ds_write_b128 v4, v[10:13] offset:16896
	s_waitcnt vmcnt(3)
	ds_write_b128 v5, v[14:17]
	s_waitcnt vmcnt(2)
	ds_write_b128 v5, v[18:21] offset:16384
	s_waitcnt vmcnt(1)
	ds_write_b128 v5, v[22:25] offset:32768
	s_waitcnt vmcnt(0)
	ds_write_b128 v5, v[26:29] offset:49152
	v_add_u32_e32 v38, 0x1cc90, v30
	s_and_saveexec_b64 s[4:5], vcc
	ds_write_b128 v38, v[34:37]
	s_mov_b64 exec, s[4:5]
	v_cmp_gt_u32_e32 vcc, 64, v0
	s_and_saveexec_b64 s[4:5], vcc
	v_lshl_add_u32 v1, v0, 1, 0
	v_add_u32_e32 v1, 0x1cc10, v1
	v_mov_b32_e32 v2, 0
	ds_write_b16 v1, v2
	s_or_b64 exec, exec, s[4:5]
	s_mov_b32 s4, 0
	v_cmp_eq_u32_e32 vcc, 0, v0
	s_and_saveexec_b64 s[6:7], vcc
	v_mov_b32_e32 v1, 0
	ds_write_b32 v1, v1 offset:52224
	s_or_b64 exec, exec, s[6:7]
	s_waitcnt lgkmcnt(0)
	s_barrier
	s_mul_i32 s8, s2, 0x186a0
	s_lshr_b32 s8, s8, 8
	s_add_i32 s3, s2, 1
	s_mul_i32 s18, s3, 0x186a0
	s_lshr_b32 s18, s18, 8

.LBB4_103:
	s_endpgm
	.p2align	8

_Z7k_layerILi2EEvPKDF16_PKiPKjS3_S3_S1_PKfPDF16_PhS3_S7_Pf:
	s_load_dwordx2 s[24:25], s[0:1], 0x58
	s_load_dwordx4 s[12:15], s[0:1], 0x0
	s_load_dwordx2 s[26:27], s[0:1], 0x10
	s_load_dwordx4 s[16:19], s[0:1], 0x48
	s_load_dwordx4 s[20:23], s[0:1], 0x28
	v_lshrrev_b32_e32 v2, 5, v0
	v_and_b32_e32 v4, 31, v0
	v_mul_u32_u24_e32 v3, 0x210, v2
	v_lshlrev_b32_e32 v5, 4, v4
	v_add3_u32 v4, v3, v5, 0
	v_lshl_or_b32 v2, v2, 9, v5
	v_mov_b32_e32 v3, 0
	v_or_b32_e32 v1, 0xfffffc00, v0
	s_waitcnt lgkmcnt(0)
	v_add_u32_e32 v3, 0x4000, v2
	v_lshlrev_b32_e32 v14, 4, v0
	v_add_u32_e32 v15, 0xffffff00, v14
	s_mov_b64 s[4:5], exec
	v_cmp_gt_u32_e32 vcc, 16, v0
	v_cmp_gt_u32_e64 s[6:7], 48, v0
	s_andn2_b64 s[8:9], s[6:7], vcc
	s_and_b64 exec, s[4:5], vcc
	global_load_dwordx4 v[16:19], v14, s[22:23]
	s_and_b64 exec, s[4:5], s[8:9]
	global_load_dwordx4 v[16:19], v15, s[18:19]
	s_mov_b64 exec, s[4:5]
	global_load_dwordx4 v[6:9], v2, s[20:21]
	global_load_dwordx4 v[10:13], v3, s[20:21]
	s_waitcnt vmcnt(1)
	ds_write_b128 v4, v[6:9]
	s_waitcnt vmcnt(0)
	ds_write_b128 v4, v[10:13] offset:16896
	s_and_b64 exec, s[4:5], s[6:7]
	ds_write_b128 v14, v[16:19] offset:52240
	s_mov_b64 exec, s[4:5]
	s_mov_b32 s4, 0
	v_cmp_eq_u32_e32 vcc, 0, v0
	s_and_saveexec_b64 s[6:7], vcc
	v_mov_b32_e32 v1, 0
	ds_write_b32 v1, v1 offset:52224
	s_or_b64 exec, exec, s[6:7]
	s_waitcnt lgkmcnt(0)
	s_barrier
	s_mul_i32 s20, s2, 0x186a0
	s_lshr_b32 s20, s20, 8
	s_add_i32 s3, s2, 1
	s_mul_i32 s28, s3, 0x186a0
	s_lshr_b32 s28, s28, 8
